# conv_queue weight-conversion loop: no per-load scale wait (scales carried in regs, applied at consumption), loads waited with vmcnt(2) after the transposition
# speedup vs baseline: 1.0259x; 1.0010x over previous
.LBB0_1825:
	s_or_b64 exec, exec, s[22:23]
	s_and_b64 s[0:1], exec, s[0:1]
	v_add_u32_e32 v18, v39, v51
	s_or_b64 s[20:21], s[0:1], s[20:21]
	v_mad_u64_u32 v[12:13], s[0:1], v42, v18, 0
	v_mov_b32_e32 v2, v13
	v_mad_u64_u32 v[18:19], s[0:1], v43, v18, v[2:3]
	v_mov_b32_e32 v13, v18
	ds_read2_b32 v[18:19], v53 offset1:65
	v_add_u32_e32 v2, 0x400, v53
	v_lshl_add_u64 v[12:13], v[12:13], 1, v[40:41]
	v_ashrrev_i32_e32 v39, 31, v38
	v_lshl_add_u64 v[12:13], v[38:39], 1, v[12:13]
	s_waitcnt lgkmcnt(0)
	v_cvt_pk_bf16_f32 v28, v18, v19
	ds_read2_b32 v[18:19], v53 offset0:130 offset1:195
	v_mov_b32_e32 v38, v33
	v_mov_b32_e32 v39, v32
	v_mov_b64_e32 v[42:43], v[16:17]
	v_mov_b64_e32 v[40:41], v[14:15]
	s_waitcnt lgkmcnt(0)
	v_cvt_pk_bf16_f32 v29, v18, v19
	ds_read2_b32 v[18:19], v2 offset0:4 offset1:69
	s_waitcnt lgkmcnt(0)
	v_cvt_pk_bf16_f32 v30, v18, v19
	ds_read2_b32 v[18:19], v2 offset0:134 offset1:199
	v_add_u32_e32 v2, 0x400, v54
	s_waitcnt lgkmcnt(0)
	v_cvt_pk_bf16_f32 v31, v18, v19
	v_lshl_add_u64 v[18:19], v[44:45], 1, v[12:13]
	global_store_dwordx4 v[18:19], v[28:31], off
	ds_read2_b32 v[18:19], v54 offset1:65
	v_lshl_add_u64 v[12:13], v[46:47], 1, v[12:13]
	s_waitcnt lgkmcnt(0)
	v_cvt_pk_bf16_f32 v28, v18, v19
	ds_read2_b32 v[18:19], v54 offset0:130 offset1:195
	s_waitcnt lgkmcnt(0)
	v_cvt_pk_bf16_f32 v29, v18, v19
	ds_read2_b32 v[18:19], v2 offset0:4 offset1:69
	s_waitcnt lgkmcnt(0)
	v_cvt_pk_bf16_f32 v30, v18, v19
	ds_read2_b32 v[18:19], v2 offset0:134 offset1:199
	s_waitcnt lgkmcnt(0)
	v_cvt_pk_bf16_f32 v31, v18, v19
	global_store_dwordx4 v[12:13], v[28:31], off
	s_waitcnt vmcnt(2)
	v_pk_mul_f32 v[4:5], v[4:5], v[238:239] op_sel_hi:[1,0]
	v_pk_mul_f32 v[6:7], v[6:7], v[238:239] op_sel_hi:[1,0]
	v_pk_mul_f32 v[8:9], v[8:9], v[240:241] op_sel_hi:[1,0]
	v_pk_mul_f32 v[10:11], v[10:11], v[240:241] op_sel_hi:[1,0]
	v_pk_mul_f32 v[20:21], v[20:21], v[242:243] op_sel_hi:[1,0]
	v_pk_mul_f32 v[22:23], v[22:23], v[242:243] op_sel_hi:[1,0]
	v_pk_mul_f32 v[24:25], v[24:25], v[244:245] op_sel_hi:[1,0]
	v_pk_mul_f32 v[26:27], v[26:27], v[244:245] op_sel_hi:[1,0]
	v_mov_b32_e32 v16, v4
	v_mov_b32_e32 v17, v5
	v_mov_b32_e32 v14, v10
	v_mov_b32_e32 v15, v11
	v_mov_b32_e32 v32, v20
	v_mov_b32_e32 v33, v21
	v_mov_b32_e32 v34, v22
	v_mov_b32_e32 v35, v23
	v_mov_b32_e32 v18, v6
	v_mov_b32_e32 v19, v7
	v_mov_b32_e32 v12, v8
	v_mov_b32_e32 v13, v9
	v_mov_b32_e32 v28, v24
	v_mov_b32_e32 v29, v25
	v_mov_b32_e32 v30, v26
	v_mov_b32_e32 v31, v27
	s_barrier
	s_andn2_b64 exec, exec, s[20:21]
	s_cbranch_execz .LBB0_1912

.LBB0_1897:
	s_or_b64 exec, exec, s[4:5]
	v_cmp_ne_u64_e64 s[2:3], 0, v[12:13]
	v_mov_b32_e32 v8, 0
	v_mov_b32_e32 v4, 0
	v_mov_b32_e32 v5, 0
	v_mov_b32_e32 v6, 0
	v_mov_b32_e32 v7, 0
	v_mov_b32_e32 v238, 1.0
	s_and_saveexec_b64 s[26:27], s[2:3]
	s_cbranch_execz .LBB0_1901
	v_add_u32_e32 v10, v33, v37
	v_ashrrev_i32_e32 v11, 31, v10
	v_mul_lo_u32 v2, v18, v11
	v_mul_lo_u32 v6, v19, v10
	v_mad_u64_u32 v[4:5], s[4:5], v18, v10, 0
	v_add3_u32 v5, v5, v2, v6
	v_lshl_add_u64 v[4:5], v[4:5], 2, v[12:13]
	global_load_dwordx4 v[4:7], v[4:5], off
	v_cmp_ne_u64_e64 s[4:5], 0, v[28:29]
	s_and_saveexec_b64 s[28:29], s[4:5]
	s_cbranch_execz .LBB0_1900
	v_lshl_add_u64 v[10:11], v[10:11], 2, v[28:29]
	global_load_dword v238, v[10:11], off

.LBB0_1901:
	s_or_b64 exec, exec, s[26:27]
	v_mov_b32_e32 v9, 0
	v_mov_b32_e32 v10, 0
	v_mov_b32_e32 v11, 0
	v_mov_b32_e32 v240, 1.0
	s_and_saveexec_b64 s[26:27], s[2:3]
	s_cbranch_execz .LBB0_1905
	v_add_u32_e32 v20, v33, v48
	v_ashrrev_i32_e32 v21, 31, v20
	v_mul_lo_u32 v2, v18, v21
	v_mul_lo_u32 v10, v19, v20
	v_mad_u64_u32 v[8:9], s[4:5], v18, v20, 0
	v_add3_u32 v9, v9, v2, v10
	v_lshl_add_u64 v[8:9], v[8:9], 2, v[12:13]
	global_load_dwordx4 v[8:11], v[8:9], off
	v_cmp_ne_u64_e64 s[4:5], 0, v[28:29]
	s_and_saveexec_b64 s[28:29], s[4:5]
	s_cbranch_execz .LBB0_1904
	v_lshl_add_u64 v[20:21], v[20:21], 2, v[28:29]
	global_load_dword v240, v[20:21], off

.LBB0_1905:
	s_or_b64 exec, exec, s[26:27]
	v_mov_b32_e32 v24, 0
	v_mov_b32_e32 v20, 0
	v_mov_b32_e32 v21, 0
	v_mov_b32_e32 v22, 0
	v_mov_b32_e32 v23, 0
	v_mov_b32_e32 v242, 1.0
	s_and_saveexec_b64 s[26:27], s[2:3]
	s_cbranch_execz .LBB0_1909
	v_add_u32_e32 v26, v33, v49
	v_ashrrev_i32_e32 v27, 31, v26
	v_mul_lo_u32 v2, v18, v27
	v_mul_lo_u32 v22, v19, v26
	v_mad_u64_u32 v[20:21], s[4:5], v18, v26, 0
	v_add3_u32 v21, v21, v2, v22
	v_lshl_add_u64 v[20:21], v[20:21], 2, v[12:13]
	global_load_dwordx4 v[20:23], v[20:21], off
	v_cmp_ne_u64_e64 s[4:5], 0, v[28:29]
	s_and_saveexec_b64 s[28:29], s[4:5]
	s_cbranch_execz .LBB0_1908
	v_lshl_add_u64 v[26:27], v[26:27], 2, v[28:29]
	global_load_dword v242, v[26:27], off

.LBB0_1909:
	s_or_b64 exec, exec, s[26:27]
	v_mov_b32_e32 v25, 0
	v_mov_b32_e32 v26, 0
	v_mov_b32_e32 v27, 0
	v_mov_b32_e32 v244, 1.0
	s_and_saveexec_b64 s[4:5], s[2:3]
	s_cbranch_execz .LBB0_1824
	v_add_u32_e32 v30, v33, v50
	v_ashrrev_i32_e32 v31, 31, v30
	v_mul_lo_u32 v2, v18, v31
	v_mul_lo_u32 v24, v19, v30
	v_mad_u64_u32 v[18:19], s[2:3], v18, v30, 0
	v_add3_u32 v19, v19, v2, v24
	v_lshl_add_u64 v[12:13], v[18:19], 2, v[12:13]
	global_load_dwordx4 v[24:27], v[12:13], off
	v_cmp_ne_u64_e64 s[2:3], 0, v[28:29]
	s_and_saveexec_b64 s[26:27], s[2:3]
	s_cbranch_execz .LBB0_1823
	v_lshl_add_u64 v[12:13], v[30:31], 2, v[28:29]
	global_load_dword v244, v[12:13], off
	s_branch .LBB0_1823
